# compact shared selection-mask loop + one pad s_nop before the attention phase (byte phase 4 mod 8)
# speedup vs baseline: 1.0024x; 1.0002x over previous
.LBB0_1439:
	s_nop 0
	v_readlane_b32 s65, v255, 19
	v_readlane_b32 s94, v254, 57
	s_add_i32 s33, s65, 2
	v_readlane_b32 s95, v254, 58
	s_cmp_ge_i32 s33, s95
	s_cbranch_scc1 .LBB0_1452
	s_waitcnt vmcnt(0)
	s_barrier
	s_mov_b64 s[0:1], exec
	v_readlane_b32 s4, v254, 5
	v_readlane_b32 s5, v254, 6
	v_readlane_b32 s92, v254, 55
	v_readlane_b32 s68, v255, 17
	s_and_b64 s[4:5], s[0:1], s[4:5]
	v_readlane_b32 s93, v254, 56
	v_readlane_b32 s96, v254, 59
	v_readlane_b32 s91, v255, 21
	v_readlane_b32 s76, v255, 22
	v_readlane_b32 s69, v255, 18
	v_readlane_b32 s45, v255, 20
	s_mov_b64 exec, s[4:5]
	s_cbranch_execz .LBB0_1485
	v_readlane_b32 s4, v254, 2
	v_readlane_b32 s6, v254, 39
	v_readlane_b32 s5, v254, 3
	v_readlane_b32 s42, v254, 4
	v_mov_b32_e32 v2, s6
	s_waitcnt vmcnt(0) expcnt(0) lgkmcnt(0)
	ds_read_b32 v4, v2
	v_readlane_b32 s6, v254, 40
	s_waitcnt lgkmcnt(0)
	v_cmp_ne_u32_e32 vcc, 0, v4
	v_mov_b32_e32 v2, s6
	ds_read_b32 v2, v2
	s_cbranch_vccnz .LBB0_1456
	v_readlane_b32 s6, v254, 0
	v_readlane_b32 s7, v254, 1
	s_load_dwordx2 s[12:13], s[6:7], 0x4
	s_add_u32 s6, s4, 0x1000
	s_addc_u32 s7, s5, 0
	s_add_u32 s10, s4, 0x1100
	s_addc_u32 s11, s5, 0
	s_waitcnt lgkmcnt(0)
	s_mul_i32 s36, s12, s3
	s_add_u32 s12, s4, 0x1200
	s_mul_i32 s36, s36, s13
	s_addc_u32 s13, s5, 0
	s_add_u32 s14, s4, 0x1300
	s_addc_u32 s15, s5, 0
	s_mov_b32 s37, 1
	s_mov_b64 s[16:17], 0
	s_branch .LBB0_1445
